# P2 pipelined + one mid-arrival CU per XCD issues an early L2 write-back at each grid barrier
# speedup vs baseline: 1.0070x; 1.0070x over previous
.LBB0_66:
	s_or_b64 exec, exec, s[6:7]
	v_cvt_f32_u32_e32 v5, v3
	s_waitcnt vmcnt(0)
	v_readfirstlane_b32 s4, v4
	s_nop 0
	s_and_b32 s98, s4, 31
	s_cmp_eq_u32 s98, 15
	s_cbranch_scc0 .Lwbskip_0
	buffer_wbl2 sc1
.Lwbskip_0:
	v_sub_u32_e32 v4, 0, v3
	v_rcp_iflag_f32_e32 v5, v5
	v_add_u32_e32 v6, s4, v2
	v_mul_f32_e32 v5, 0x4f7ffffe, v5
	v_cvt_u32_f32_e32 v5, v5
	v_mul_lo_u32 v2, v4, v5
	v_mul_hi_u32 v2, v5, v2
	v_add_u32_e32 v2, v5, v2
	v_mul_hi_u32 v2, v6, v2
	v_mul_lo_u32 v4, v2, v3
	v_sub_u32_e32 v4, v6, v4
	v_add_u32_e32 v5, 1, v2
	v_cmp_ge_u32_e32 vcc, v4, v3
	s_nop 1
	v_cndmask_b32_e32 v2, v2, v5, vcc
	v_sub_u32_e32 v5, v4, v3
	v_cndmask_b32_e32 v4, v4, v5, vcc
	v_add_u32_e32 v5, 1, v2
	v_cmp_ge_u32_e32 vcc, v4, v3
	v_add_u32_e32 v4, 1, v6
	s_nop 0
	v_cndmask_b32_e32 v2, v2, v5, vcc
	v_mul_lo_u32 v5, v3, v2
	v_add_u32_e32 v3, v5, v3
	v_cmp_ne_u32_e32 vcc, v4, v3
	s_and_saveexec_b64 s[4:5], vcc
	s_xor_b64 s[4:5], exec, s[4:5]
	s_cbranch_execz .LBB0_80
	s_waitcnt lgkmcnt(0)
	v_mov_b32_e32 v1, 0x2000
	global_load_dword v1, v1, s[2:3] offset:1024 sc1
	s_add_u32 s10, s2, 0x2400
	s_addc_u32 s11, s3, 0
	s_waitcnt vmcnt(0)
	v_cmp_eq_u32_e32 vcc, v1, v2
	s_and_saveexec_b64 s[6:7], vcc
	s_cbranch_execz .LBB0_79
	v_readlane_b32 s8, v255, 2
	v_readlane_b32 s9, v255, 3
	s_add_u32 s8, s8, 0x4200
	s_addc_u32 s9, s9, 0
	s_mov_b32 s22, 1
	s_mov_b64 s[12:13], 0
	v_mov_b32_e32 v1, 0
	s_branch .LBB0_70

.LBB0_403:
	s_or_b64 exec, exec, s[6:7]
	v_cvt_f32_u32_e32 v6, v4
	s_waitcnt vmcnt(0)
	v_readfirstlane_b32 s4, v5
	s_nop 0
	s_and_b32 s98, s4, 31
	s_cmp_eq_u32 s98, 15
	s_cbranch_scc0 .Lwbskip_3
	buffer_wbl2 sc1
.Lwbskip_3:
	v_sub_u32_e32 v5, 0, v4
	v_rcp_iflag_f32_e32 v6, v6
	v_add_u32_e32 v7, s4, v3
	v_mul_f32_e32 v6, 0x4f7ffffe, v6
	v_cvt_u32_f32_e32 v6, v6
	v_mul_lo_u32 v3, v5, v6
	v_mul_hi_u32 v3, v6, v3
	v_add_u32_e32 v3, v6, v3
	v_mul_hi_u32 v3, v7, v3
	v_mul_lo_u32 v5, v3, v4
	v_sub_u32_e32 v5, v7, v5
	v_add_u32_e32 v6, 1, v3
	v_cmp_ge_u32_e32 vcc, v5, v4
	s_nop 1
	v_cndmask_b32_e32 v3, v3, v6, vcc
	v_sub_u32_e32 v6, v5, v4
	v_cndmask_b32_e32 v5, v5, v6, vcc
	v_add_u32_e32 v6, 1, v3
	v_cmp_ge_u32_e32 vcc, v5, v4
	v_add_u32_e32 v5, 1, v7
	s_nop 0
	v_cndmask_b32_e32 v3, v3, v6, vcc
	v_mul_lo_u32 v6, v4, v3
	v_add_u32_e32 v4, v6, v4
	v_cmp_ne_u32_e32 vcc, v5, v4
	s_and_saveexec_b64 s[4:5], vcc
	s_xor_b64 s[4:5], exec, s[4:5]
	s_cbranch_execz .LBB0_417
	s_waitcnt lgkmcnt(0)
	v_mov_b32_e32 v2, 0x2000
	global_load_dword v2, v2, s[2:3] offset:1024 sc1
	s_add_u32 s10, s2, 0x2400
	s_addc_u32 s11, s3, 0
	s_waitcnt vmcnt(0)
	v_cmp_eq_u32_e32 vcc, v2, v3
	s_and_saveexec_b64 s[6:7], vcc
	s_cbranch_execz .LBB0_416
	v_readlane_b32 s8, v255, 2
	v_readlane_b32 s9, v255, 3
	s_add_u32 s8, s8, 0x4200
	s_addc_u32 s9, s9, 0
	s_mov_b32 s22, 1
	s_mov_b64 s[12:13], 0
	v_mov_b32_e32 v2, 0
	s_branch .LBB0_407

.Lwbskip_4:
	v_sub_u32_e32 v5, 0, v4
	v_rcp_iflag_f32_e32 v6, v6
	v_add_u32_e32 v7, s4, v3
	v_mul_f32_e32 v6, 0x4f7ffffe, v6
	v_cvt_u32_f32_e32 v6, v6
	v_mul_lo_u32 v3, v5, v6
	v_mul_hi_u32 v3, v6, v3
	v_add_u32_e32 v3, v6, v3
	v_mul_hi_u32 v3, v7, v3
	v_mul_lo_u32 v5, v3, v4
	v_sub_u32_e32 v5, v7, v5
	v_add_u32_e32 v6, 1, v3
	v_cmp_ge_u32_e32 vcc, v5, v4
	s_nop 1
	v_cndmask_b32_e32 v3, v3, v6, vcc
	v_sub_u32_e32 v6, v5, v4
	v_cndmask_b32_e32 v5, v5, v6, vcc
	v_add_u32_e32 v6, 1, v3
	v_cmp_ge_u32_e32 vcc, v5, v4
	v_add_u32_e32 v5, 1, v7
	s_nop 0
	v_cndmask_b32_e32 v3, v3, v6, vcc
	v_mul_lo_u32 v6, v4, v3
	v_add_u32_e32 v4, v6, v4
	v_cmp_ne_u32_e32 vcc, v5, v4
	s_and_saveexec_b64 s[4:5], vcc
	s_xor_b64 s[4:5], exec, s[4:5]
	s_cbranch_execz .LBB0_509
	s_waitcnt lgkmcnt(0)
	v_mov_b32_e32 v2, 0x2000
	global_load_dword v2, v2, s[2:3] offset:1024 sc1
	s_add_u32 s12, s2, 0x2400
	s_addc_u32 s13, s3, 0
	s_waitcnt vmcnt(0)
	v_cmp_eq_u32_e32 vcc, v2, v3
	s_and_saveexec_b64 s[6:7], vcc
	s_cbranch_execz .LBB0_508
	v_readlane_b32 s10, v255, 2
	v_readlane_b32 s11, v255, 3
	s_add_u32 s10, s10, 0x4200
	s_addc_u32 s11, s11, 0
	s_mov_b32 s24, 1
	s_mov_b64 s[14:15], 0
	v_mov_b32_e32 v2, 0
	s_branch .LBB0_499

.Lwbskip_6:
	v_sub_u32_e32 v4, 0, v3
	v_rcp_iflag_f32_e32 v5, v5
	v_add_u32_e32 v6, s4, v2
	v_mul_f32_e32 v5, 0x4f7ffffe, v5
	v_cvt_u32_f32_e32 v5, v5
	v_mul_lo_u32 v2, v4, v5
	v_mul_hi_u32 v2, v5, v2
	v_add_u32_e32 v2, v5, v2
	v_mul_hi_u32 v2, v6, v2
	v_mul_lo_u32 v4, v2, v3
	v_sub_u32_e32 v4, v6, v4
	v_add_u32_e32 v5, 1, v2
	v_cmp_ge_u32_e32 vcc, v4, v3
	s_nop 1
	v_cndmask_b32_e32 v2, v2, v5, vcc
	v_sub_u32_e32 v5, v4, v3
	v_cndmask_b32_e32 v4, v4, v5, vcc
	v_add_u32_e32 v5, 1, v2
	v_cmp_ge_u32_e32 vcc, v4, v3
	v_add_u32_e32 v4, 1, v6
	s_nop 0
	v_cndmask_b32_e32 v2, v2, v5, vcc
	v_mul_lo_u32 v5, v3, v2
	v_add_u32_e32 v3, v5, v3
	v_cmp_ne_u32_e32 vcc, v4, v3
	s_and_saveexec_b64 s[4:5], vcc
	s_xor_b64 s[4:5], exec, s[4:5]
	s_cbranch_execz .LBB0_687
	s_waitcnt lgkmcnt(0)
	v_mov_b32_e32 v1, 0x2000
	global_load_dword v1, v1, s[2:3] offset:1024 sc1
	s_add_u32 s12, s2, 0x2400
	s_addc_u32 s13, s3, 0
	s_waitcnt vmcnt(0)
	v_cmp_eq_u32_e32 vcc, v1, v2
	s_and_saveexec_b64 s[6:7], vcc
	s_cbranch_execz .LBB0_686
	v_readlane_b32 s10, v255, 2
	v_readlane_b32 s11, v255, 3
	s_add_u32 s10, s10, 0x4200
	s_addc_u32 s11, s11, 0
	s_mov_b32 s24, 1
	s_mov_b64 s[14:15], 0
	v_mov_b32_e32 v1, 0
	s_branch .LBB0_677

.LBB0_749:
	s_or_b64 exec, exec, s[6:7]
	v_cvt_f32_u32_e32 v4, v2
	s_waitcnt vmcnt(0)
	v_readfirstlane_b32 s4, v3
	s_nop 0
	s_and_b32 s98, s4, 31
	s_cmp_eq_u32 s98, 15
	s_cbranch_scc0 .Lwbskip_7
	buffer_wbl2 sc1
.Lwbskip_7:
	v_sub_u32_e32 v3, 0, v2
	v_rcp_iflag_f32_e32 v4, v4
	v_add_u32_e32 v5, s4, v1
	v_mul_f32_e32 v4, 0x4f7ffffe, v4
	v_cvt_u32_f32_e32 v4, v4
	v_mul_lo_u32 v1, v3, v4
	v_mul_hi_u32 v1, v4, v1
	v_add_u32_e32 v1, v4, v1
	v_mul_hi_u32 v1, v5, v1
	v_mul_lo_u32 v3, v1, v2
	v_sub_u32_e32 v3, v5, v3
	v_add_u32_e32 v4, 1, v1
	v_cmp_ge_u32_e32 vcc, v3, v2
	s_nop 1
	v_cndmask_b32_e32 v1, v1, v4, vcc
	v_sub_u32_e32 v4, v3, v2
	v_cndmask_b32_e32 v3, v3, v4, vcc
	v_add_u32_e32 v4, 1, v1
	v_cmp_ge_u32_e32 vcc, v3, v2
	v_add_u32_e32 v3, 1, v5
	s_nop 0
	v_cndmask_b32_e32 v1, v1, v4, vcc
	v_mul_lo_u32 v4, v2, v1
	v_add_u32_e32 v2, v4, v2
	v_cmp_ne_u32_e32 vcc, v3, v2
	s_and_saveexec_b64 s[4:5], vcc
	s_xor_b64 s[4:5], exec, s[4:5]
	s_cbranch_execz .LBB0_763
	s_waitcnt lgkmcnt(0)
	v_mov_b32_e32 v0, 0x2000
	global_load_dword v0, v0, s[2:3] offset:1024 sc1
	s_add_u32 s10, s2, 0x2400
	s_addc_u32 s11, s3, 0
	s_waitcnt vmcnt(0)
	v_cmp_eq_u32_e32 vcc, v0, v1
	s_and_saveexec_b64 s[6:7], vcc
	s_cbranch_execz .LBB0_762
	v_readlane_b32 s8, v255, 2
	v_readlane_b32 s9, v255, 3
	s_add_u32 s8, s8, 0x4200
	s_addc_u32 s9, s9, 0
	s_mov_b32 s22, 1
	s_mov_b64 s[12:13], 0
	v_mov_b32_e32 v0, 0
	s_branch .LBB0_753

	.amdhsa_kernel _Z6mk_fwd4Args
		.amdhsa_group_segment_fixed_size 0
		.amdhsa_private_segment_fixed_size 0
		.amdhsa_kernarg_size 472
		.amdhsa_user_sgpr_count 2
		.amdhsa_user_sgpr_dispatch_ptr 0
		.amdhsa_user_sgpr_queue_ptr 0
		.amdhsa_user_sgpr_kernarg_segment_ptr 1
		.amdhsa_user_sgpr_dispatch_id 0
		.amdhsa_user_sgpr_kernarg_preload_length 0
		.amdhsa_user_sgpr_kernarg_preload_offset 0
		.amdhsa_user_sgpr_private_segment_size 0
		.amdhsa_uses_dynamic_stack 0
		.amdhsa_enable_private_segment 0
		.amdhsa_system_sgpr_workgroup_id_x 1
		.amdhsa_system_sgpr_workgroup_id_y 0
		.amdhsa_system_sgpr_workgroup_id_z 0
		.amdhsa_system_sgpr_workgroup_info 0
		.amdhsa_system_vgpr_workitem_id 0
		.amdhsa_next_free_vgpr 256
		.amdhsa_next_free_sgpr 102
		.amdhsa_accum_offset 256
		.amdhsa_reserve_vcc 1
		.amdhsa_float_round_mode_32 0
		.amdhsa_float_round_mode_16_64 0
		.amdhsa_float_denorm_mode_32 3
		.amdhsa_float_denorm_mode_16_64 3
		.amdhsa_dx10_clamp 1
		.amdhsa_ieee_mode 1
		.amdhsa_fp16_overflow 0
		.amdhsa_tg_split 0
		.amdhsa_exception_fp_ieee_invalid_op 0
		.amdhsa_exception_fp_denorm_src 0
		.amdhsa_exception_fp_ieee_div_zero 0
		.amdhsa_exception_fp_ieee_overflow 0
		.amdhsa_exception_fp_ieee_underflow 0
		.amdhsa_exception_fp_ieee_inexact 0
		.amdhsa_exception_int_div_zero 0
	.end_amdhsa_kernel

amdhsa.kernels:
  - .agpr_count:     0
    .args:
      - .offset:         0
        .size:           216
        .value_kind:     by_value
      - .offset:         216
        .size:           4
        .value_kind:     hidden_block_count_x
      - .offset:         220
        .size:           4
        .value_kind:     hidden_block_count_y
      - .offset:         224
        .size:           4
        .value_kind:     hidden_block_count_z
      - .offset:         228
        .size:           2
        .value_kind:     hidden_group_size_x
      - .offset:         230
        .size:           2
        .value_kind:     hidden_group_size_y
      - .offset:         232
        .size:           2
        .value_kind:     hidden_group_size_z
      - .offset:         234
        .size:           2
        .value_kind:     hidden_remainder_x
      - .offset:         236
        .size:           2
        .value_kind:     hidden_remainder_y
      - .offset:         238
        .size:           2
        .value_kind:     hidden_remainder_z
      - .offset:         256
        .size:           8
        .value_kind:     hidden_global_offset_x
      - .offset:         264
        .size:           8
        .value_kind:     hidden_global_offset_y
      - .offset:         272
        .size:           8
        .value_kind:     hidden_global_offset_z
      - .offset:         280
        .size:           2
        .value_kind:     hidden_grid_dims
      - .offset:         336
        .size:           4
        .value_kind:     hidden_dynamic_lds_size
    .group_segment_fixed_size: 0
    .kernarg_segment_align: 8
    .kernarg_segment_size: 472
    .language:       OpenCL C
    .language_version:
      - 2
      - 0
    .max_flat_workgroup_size: 512
    .name:           _Z6mk_fwd4Args
    .private_segment_fixed_size: 0
    .sgpr_count:     108
    .sgpr_spill_count: 55
    .symbol:         _Z6mk_fwd4Args.kd
    .uniform_work_group_size: 1
    .uses_dynamic_stack: false
    .vgpr_count:     256
    .vgpr_spill_count: 0
    .wavefront_size: 64
